# grid barrier: workgroups that are not XCD-last poll the generation word with two staggered loads in flight (vmcnt(1) pipelining) instead of one poll per round trip
# speedup vs baseline: 1.0028x; 1.0028x over previous
.LBB0_66:
	v_readlane_b32 s0, v254, 6
	s_lshl_b32 s0, s0, 8
	v_readlane_b32 s2, v254, 4
	v_readlane_b32 s3, v254, 5
	s_add_u32 s6, s2, s0
	s_addc_u32 s7, s3, 0
	v_mov_b32_e32 v1, 0x1000
	v_mov_b32_e32 v3, 1
	global_atomic_add v3, v1, v3, s[6:7] offset:1024 sc0
	v_cvt_f32_u32_e32 v1, v2
	v_sub_u32_e32 v4, 0, v2
	v_rcp_iflag_f32_e32 v1, v1
	s_nop 0
	v_mul_f32_e32 v1, 0x4f7ffffe, v1
	v_cvt_u32_f32_e32 v1, v1
	v_mul_lo_u32 v4, v4, v1
	v_mul_hi_u32 v4, v1, v4
	v_add_u32_e32 v1, v1, v4
	s_waitcnt vmcnt(0)
	v_mul_hi_u32 v1, v3, v1
	v_mul_lo_u32 v4, v1, v2
	v_sub_u32_e32 v4, v3, v4
	v_add_u32_e32 v5, 1, v1
	v_cmp_ge_u32_e32 vcc, v4, v2
	v_add_u32_e32 v3, 1, v3
	s_nop 0
	v_cndmask_b32_e32 v1, v1, v5, vcc
	v_sub_u32_e32 v5, v4, v2
	v_cndmask_b32_e32 v4, v4, v5, vcc
	v_add_u32_e32 v5, 1, v1
	v_cmp_ge_u32_e32 vcc, v4, v2
	s_nop 1
	v_cndmask_b32_e32 v1, v1, v5, vcc
	v_mul_lo_u32 v4, v2, v1
	v_add_u32_e32 v2, v4, v2
	v_cmp_ne_u32_e32 vcc, v3, v2
	s_and_saveexec_b64 s[0:1], vcc
	s_xor_b64 s[8:9], exec, s[0:1]
	s_cbranch_execz .LBB0_80
	s_waitcnt lgkmcnt(0)
	s_add_u32 s14, s26, 0x7500
	s_addc_u32 s15, s27, 0
	v_mov_b32_e32 v0, 0
	s_mov_b64 s[10:11], exec
	global_load_dword v2, v0, s[14:15] sc1
	s_sleep 24
	global_load_dword v3, v0, s[14:15] sc1
.Lbsp_0:
	s_waitcnt vmcnt(1)
	v_cmp_ne_u32_e32 vcc, v2, v1
	s_cbranch_vccnz .Lbsd_0
	global_load_dword v2, v0, s[14:15] sc1
	s_waitcnt vmcnt(1)
	v_cmp_ne_u32_e32 vcc, v3, v1
	s_cbranch_vccnz .Lbsd_0
	global_load_dword v3, v0, s[14:15] sc1
	s_branch .Lbsp_0
.Lbsd_0:
	s_branch .LBB0_79
	s_add_u32 s12, s26, 0x4200
	s_addc_u32 s13, s27, 0
	s_mov_b32 s0, 1
	s_mov_b64 s[16:17], 0
	v_mov_b32_e32 v0, 0
	s_branch .LBB0_70
